# memory-K/V staging loads all in flight + FMA loop weight rows prefetched one step ahead; helper CUs convert all x rows (transposing CUs none)
# baseline (speedup 1.0000x reference)
.LBB0_898:
	s_lshl_b32 s8, s43, 3
	s_add_i32 s8, s8, s91
	s_lshl_b32 s10, s42, 3
	s_movk_i32 s99, 0x3fff
	s_cmp_lg_u32 s42, 0x100
	s_cbranch_scc1 .Lp0_xs_done
	s_and_b32 s98, s43, 31
	s_lshr_b32 s8, s43, 5
	s_cmp_lt_u32 s98, 8
	s_cbranch_scc1 .Lp0_xs_B
	s_mul_i32 s8, s8, 24
	s_add_i32 s8, s8, s98
	s_add_i32 s8, s8, -8
	s_lshl_b32 s8, s8, 3
	s_add_i32 s8, s8, s91
	s_addk_i32 s8, 0x4000
	s_movk_i32 s10, 0x600
	s_branch .Lp0_xs_done
.Lp0_xs_B:
	s_mul_i32 s8, s8, 8
	s_add_i32 s8, s8, s98
	s_lshl_b32 s8, s8, 3
	s_add_i32 s8, s8, s91
	s_movk_i32 s10, 0x200
	s_movk_i32 s99, 0x3fff

.LBB0_936:
	v_ashrrev_i32_e32 v42, 9, v38
	v_ashrrev_i32_e32 v43, 31, v42
	v_lshlrev_b64 v[44:45], 13, v[42:43]
	v_lshl_add_u64 v[44:45], v[36:37], 0, v[44:45]
	s_movk_i32 s98, 0x2000
	s_mov_b32 s99, 0
	global_load_dword v186, v[44:45], off
	v_lshl_add_u64 v[44:45], v[44:45], 0, s[98:99]
	global_load_dword v187, v[44:45], off
	v_lshl_add_u64 v[44:45], v[44:45], 0, s[98:99]
	global_load_dword v188, v[44:45], off
	v_lshl_add_u64 v[44:45], v[44:45], 0, s[98:99]
	global_load_dword v189, v[44:45], off
	v_lshl_add_u64 v[44:45], v[44:45], 0, s[98:99]
	global_load_dword v190, v[44:45], off
	v_lshl_add_u64 v[44:45], v[44:45], 0, s[98:99]
	global_load_dword v191, v[44:45], off
	v_lshl_add_u64 v[44:45], v[44:45], 0, s[98:99]
	global_load_dword v192, v[44:45], off
	v_lshl_add_u64 v[44:45], v[44:45], 0, s[98:99]
	global_load_dword v193, v[44:45], off
	v_lshl_add_u64 v[44:45], v[44:45], 0, s[98:99]
	global_load_dword v194, v[44:45], off
	v_lshl_add_u64 v[44:45], v[44:45], 0, s[98:99]
	global_load_dword v195, v[44:45], off
	v_lshl_add_u64 v[44:45], v[44:45], 0, s[98:99]
	global_load_dword v196, v[44:45], off
	v_lshl_add_u64 v[44:45], v[44:45], 0, s[98:99]
	global_load_dword v197, v[44:45], off
	v_lshl_add_u64 v[44:45], v[44:45], 0, s[98:99]
	global_load_dword v198, v[44:45], off
	v_lshl_add_u64 v[44:45], v[44:45], 0, s[98:99]
	global_load_dword v199, v[44:45], off
	v_lshl_add_u64 v[44:45], v[44:45], 0, s[98:99]
	global_load_dword v200, v[44:45], off
	v_lshl_add_u64 v[44:45], v[44:45], 0, s[98:99]
	global_load_dword v201, v[44:45], off
	v_lshl_add_u32 v42, v42, 2, v108
	s_waitcnt vmcnt(15)
	v_mul_f32_e32 v186, v186, v2
	ds_write_b32 v42, v186
	s_waitcnt vmcnt(14)
	v_mul_f32_e32 v187, v187, v2
	ds_write_b32 v42, v187 offset:4
	s_waitcnt vmcnt(13)
	v_mul_f32_e32 v188, v188, v2
	ds_write_b32 v42, v188 offset:8
	s_waitcnt vmcnt(12)
	v_mul_f32_e32 v189, v189, v2
	ds_write_b32 v42, v189 offset:12
	s_waitcnt vmcnt(11)
	v_mul_f32_e32 v190, v190, v2
	ds_write_b32 v42, v190 offset:16
	s_waitcnt vmcnt(10)
	v_mul_f32_e32 v191, v191, v2
	ds_write_b32 v42, v191 offset:20
	s_waitcnt vmcnt(9)
	v_mul_f32_e32 v192, v192, v2
	ds_write_b32 v42, v192 offset:24
	s_waitcnt vmcnt(8)
	v_mul_f32_e32 v193, v193, v2
	ds_write_b32 v42, v193 offset:28
	s_waitcnt vmcnt(7)
	v_mul_f32_e32 v194, v194, v2
	ds_write_b32 v42, v194 offset:32
	s_waitcnt vmcnt(6)
	v_mul_f32_e32 v195, v195, v2
	ds_write_b32 v42, v195 offset:36
	s_waitcnt vmcnt(5)
	v_mul_f32_e32 v196, v196, v2
	ds_write_b32 v42, v196 offset:40
	s_waitcnt vmcnt(4)
	v_mul_f32_e32 v197, v197, v2
	ds_write_b32 v42, v197 offset:44
	s_waitcnt vmcnt(3)
	v_mul_f32_e32 v198, v198, v2
	ds_write_b32 v42, v198 offset:48
	s_waitcnt vmcnt(2)
	v_mul_f32_e32 v199, v199, v2
	ds_write_b32 v42, v199 offset:52
	s_waitcnt vmcnt(1)
	v_mul_f32_e32 v200, v200, v2
	ds_write_b32 v42, v200 offset:56
	s_waitcnt vmcnt(0)
	v_mul_f32_e32 v201, v201, v2
	ds_write_b32 v42, v201 offset:60
	s_or_b64 exec, exec, s[30:31]
	s_orn2_b64 s[30:31], s[8:9], exec
	v_mov_b32_e32 v0, v110

.LBB0_941:
	s_or_b64 exec, exec, s[10:11]
	s_mov_b64 s[28:29], 0
	s_waitcnt vmcnt(0)
	v_mov_b64_e32 v[2:3], v[96:97]
	v_mov_b32_e32 v0, v111
	v_mov_b32_e32 v112, v105
	s_waitcnt lgkmcnt(0)
	s_barrier
	v_add_co_u32_e32 v218, vcc, 0xffff9000, v2
	s_nop 1
	v_addc_co_u32_e32 v219, vcc, -1, v3, vcc
	global_load_dwordx4 v[186:189], v[218:219], off
	v_add_co_u32_e32 v220, vcc, 0xffffa000, v2
	s_nop 1
	v_addc_co_u32_e32 v221, vcc, -1, v3, vcc
	global_load_dwordx4 v[190:193], v[220:221], off
	v_add_co_u32_e32 v218, vcc, 0xffffb000, v2
	s_nop 1
	v_addc_co_u32_e32 v219, vcc, -1, v3, vcc
	global_load_dwordx4 v[194:197], v[218:219], off
	v_add_co_u32_e32 v220, vcc, 0xffffc000, v2
	s_nop 1
	v_addc_co_u32_e32 v221, vcc, -1, v3, vcc
	global_load_dwordx4 v[198:201], v[220:221], off
	v_add_co_u32_e32 v218, vcc, 0xffffd000, v2
	s_nop 1
	v_addc_co_u32_e32 v219, vcc, -1, v3, vcc
	global_load_dwordx4 v[202:205], v[218:219], off
	v_add_co_u32_e32 v220, vcc, 0xffffe000, v2
	s_nop 1
	v_addc_co_u32_e32 v221, vcc, -1, v3, vcc
	global_load_dwordx4 v[206:209], v[220:221], off
	global_load_dwordx4 v[210:213], v[2:3], off offset:-4096
	global_load_dwordx4 v[214:217], v[2:3], off
.LBB0_942:
	s_waitcnt vmcnt(0)
	v_mov_b64_e32 v[130:131], v[186:187]
	v_mov_b64_e32 v[132:133], v[188:189]
	v_mov_b64_e32 v[134:135], v[190:191]
	v_mov_b64_e32 v[136:137], v[192:193]
	v_mov_b64_e32 v[138:139], v[194:195]
	v_mov_b64_e32 v[140:141], v[196:197]
	v_mov_b64_e32 v[142:143], v[198:199]
	v_mov_b64_e32 v[144:145], v[200:201]
	v_mov_b64_e32 v[146:147], v[202:203]
	v_mov_b64_e32 v[148:149], v[204:205]
	v_mov_b64_e32 v[150:151], v[206:207]
	v_mov_b64_e32 v[152:153], v[208:209]
	v_mov_b64_e32 v[40:41], v[210:211]
	v_mov_b64_e32 v[42:43], v[212:213]
	v_mov_b64_e32 v[36:37], v[214:215]
	v_mov_b64_e32 v[38:39], v[216:217]
	ds_read_b128 v[48:51], v0
	ds_read_b128 v[44:47], v0 offset:16
	ds_read_b128 v[56:59], v0 offset:64
	ds_read_b128 v[52:55], v0 offset:80
	ds_read_b128 v[64:67], v0 offset:128
	ds_read_b128 v[60:63], v0 offset:144
	ds_read_b128 v[72:75], v0 offset:192
	ds_read_b128 v[68:71], v0 offset:208
	ds_read_b128 v[80:83], v0 offset:256
	ds_read_b128 v[76:79], v0 offset:272
	ds_read_b128 v[88:91], v0 offset:320
	ds_read_b128 v[84:87], v0 offset:336
	ds_read_b128 v[114:117], v0 offset:384
	ds_read_b128 v[118:121], v0 offset:400
	ds_read_b128 v[122:125], v0 offset:448
	ds_read_b128 v[126:129], v0 offset:464
	s_waitcnt lgkmcnt(14)
	v_mov_b32_e32 v154, v51
	v_mov_b32_e32 v156, v47
	s_nop 0
	s_nop 0
	s_waitcnt lgkmcnt(13)
	v_mov_b32_e32 v158, v59
	s_nop 0
	s_waitcnt lgkmcnt(12)
	v_mov_b32_e32 v160, v55
	s_waitcnt lgkmcnt(11)
	v_mov_b32_e32 v162, v67
	s_waitcnt lgkmcnt(10)
	v_mov_b32_e32 v164, v63
	s_waitcnt lgkmcnt(9)
	v_mov_b32_e32 v166, v75
	s_waitcnt lgkmcnt(8)
	v_mov_b32_e32 v168, v71
	s_waitcnt lgkmcnt(7)
	v_mov_b32_e32 v170, v83
	s_waitcnt lgkmcnt(6)
	v_mov_b32_e32 v172, v79
	s_waitcnt lgkmcnt(5)
	v_mov_b32_e32 v174, v91
	s_waitcnt lgkmcnt(4)
	v_mov_b32_e32 v176, v87
	v_add_u32_e32 v112, 8, v112
	s_waitcnt lgkmcnt(3)
	v_mov_b32_e32 v178, v117
	s_waitcnt lgkmcnt(2)
	v_mov_b32_e32 v180, v121
	v_cmp_ge_u32_e64 s[10:11], v112, v106
	s_waitcnt lgkmcnt(1)
	v_mov_b32_e32 v182, v125
	s_waitcnt lgkmcnt(0)
	v_mov_b32_e32 v184, v129
	v_add_u32_e32 v0, 0x200, v0
	s_or_b64 s[28:29], s[10:11], s[28:29]
	v_lshl_add_u64 v[2:3], v[2:3], 0, s[22:23]
	s_mov_b64 s[98:99], exec
	s_andn2_b64 exec, exec, s[10:11]
	v_add_co_u32_e32 v218, vcc, 0xffff9000, v2
	s_nop 1
	v_addc_co_u32_e32 v219, vcc, -1, v3, vcc
	global_load_dwordx4 v[186:189], v[218:219], off
	v_add_co_u32_e32 v220, vcc, 0xffffa000, v2
	s_nop 1
	v_addc_co_u32_e32 v221, vcc, -1, v3, vcc
	global_load_dwordx4 v[190:193], v[220:221], off
	v_add_co_u32_e32 v218, vcc, 0xffffb000, v2
	s_nop 1
	v_addc_co_u32_e32 v219, vcc, -1, v3, vcc
	global_load_dwordx4 v[194:197], v[218:219], off
	v_add_co_u32_e32 v220, vcc, 0xffffc000, v2
	s_nop 1
	v_addc_co_u32_e32 v221, vcc, -1, v3, vcc
	global_load_dwordx4 v[198:201], v[220:221], off
	v_add_co_u32_e32 v218, vcc, 0xffffd000, v2
	s_nop 1
	v_addc_co_u32_e32 v219, vcc, -1, v3, vcc
	global_load_dwordx4 v[202:205], v[218:219], off
	v_add_co_u32_e32 v220, vcc, 0xffffe000, v2
	s_nop 1
	v_addc_co_u32_e32 v221, vcc, -1, v3, vcc
	global_load_dwordx4 v[206:209], v[220:221], off
	global_load_dwordx4 v[210:213], v[2:3], off offset:-4096
	global_load_dwordx4 v[214:217], v[2:3], off
	s_mov_b64 exec, s[98:99]
	v_pk_fma_f32 v[34:35], v[132:133], v[48:49], v[34:35] op_sel_hi:[1,0,1]
	v_pk_fma_f32 v[32:33], v[130:131], v[48:49], v[32:33] op_sel_hi:[1,0,1]
	v_pk_fma_f32 v[18:19], v[132:133], v[44:45], v[18:19] op_sel_hi:[1,0,1]
	v_pk_fma_f32 v[16:17], v[130:131], v[44:45], v[16:17] op_sel_hi:[1,0,1]
	v_pk_fma_f32 v[30:31], v[132:133], v[48:49], v[30:31] op_sel:[0,1,0]
	v_pk_fma_f32 v[28:29], v[130:131], v[48:49], v[28:29] op_sel:[0,1,0]
	v_pk_fma_f32 v[14:15], v[132:133], v[44:45], v[14:15] op_sel:[0,1,0]
	v_pk_fma_f32 v[12:13], v[130:131], v[44:45], v[12:13] op_sel:[0,1,0]
	v_pk_fma_f32 v[26:27], v[132:133], v[50:51], v[26:27] op_sel_hi:[1,0,1]
	v_pk_fma_f32 v[24:25], v[130:131], v[50:51], v[24:25] op_sel_hi:[1,0,1]
	v_pk_fma_f32 v[10:11], v[132:133], v[46:47], v[10:11] op_sel_hi:[1,0,1]
	v_pk_fma_f32 v[8:9], v[130:131], v[46:47], v[8:9] op_sel_hi:[1,0,1]
	v_pk_fma_f32 v[22:23], v[132:133], v[154:155], v[22:23] op_sel_hi:[1,0,1]
	v_pk_fma_f32 v[20:21], v[130:131], v[154:155], v[20:21] op_sel_hi:[1,0,1]
	v_pk_fma_f32 v[6:7], v[132:133], v[156:157], v[6:7] op_sel_hi:[1,0,1]
	v_pk_fma_f32 v[4:5], v[130:131], v[156:157], v[4:5] op_sel_hi:[1,0,1]
	v_pk_fma_f32 v[34:35], v[136:137], v[56:57], v[34:35] op_sel_hi:[1,0,1]
	v_pk_fma_f32 v[32:33], v[134:135], v[56:57], v[32:33] op_sel_hi:[1,0,1]
	v_pk_fma_f32 v[18:19], v[136:137], v[52:53], v[18:19] op_sel_hi:[1,0,1]
	v_pk_fma_f32 v[16:17], v[134:135], v[52:53], v[16:17] op_sel_hi:[1,0,1]
	v_pk_fma_f32 v[30:31], v[136:137], v[56:57], v[30:31] op_sel:[0,1,0]
	v_pk_fma_f32 v[28:29], v[134:135], v[56:57], v[28:29] op_sel:[0,1,0]
	v_pk_fma_f32 v[14:15], v[136:137], v[52:53], v[14:15] op_sel:[0,1,0]
	v_pk_fma_f32 v[12:13], v[134:135], v[52:53], v[12:13] op_sel:[0,1,0]
	v_pk_fma_f32 v[26:27], v[136:137], v[58:59], v[26:27] op_sel_hi:[1,0,1]
	v_pk_fma_f32 v[24:25], v[134:135], v[58:59], v[24:25] op_sel_hi:[1,0,1]
	v_pk_fma_f32 v[10:11], v[136:137], v[54:55], v[10:11] op_sel_hi:[1,0,1]
	v_pk_fma_f32 v[8:9], v[134:135], v[54:55], v[8:9] op_sel_hi:[1,0,1]
	v_pk_fma_f32 v[22:23], v[136:137], v[158:159], v[22:23] op_sel_hi:[1,0,1]
	v_pk_fma_f32 v[20:21], v[134:135], v[158:159], v[20:21] op_sel_hi:[1,0,1]
	v_pk_fma_f32 v[6:7], v[136:137], v[160:161], v[6:7] op_sel_hi:[1,0,1]
	v_pk_fma_f32 v[4:5], v[134:135], v[160:161], v[4:5] op_sel_hi:[1,0,1]
	v_pk_fma_f32 v[34:35], v[140:141], v[64:65], v[34:35] op_sel_hi:[1,0,1]
	v_pk_fma_f32 v[32:33], v[138:139], v[64:65], v[32:33] op_sel_hi:[1,0,1]
	v_pk_fma_f32 v[18:19], v[140:141], v[60:61], v[18:19] op_sel_hi:[1,0,1]
	v_pk_fma_f32 v[16:17], v[138:139], v[60:61], v[16:17] op_sel_hi:[1,0,1]
	v_pk_fma_f32 v[30:31], v[140:141], v[64:65], v[30:31] op_sel:[0,1,0]
	v_pk_fma_f32 v[28:29], v[138:139], v[64:65], v[28:29] op_sel:[0,1,0]
	v_pk_fma_f32 v[14:15], v[140:141], v[60:61], v[14:15] op_sel:[0,1,0]
	v_pk_fma_f32 v[12:13], v[138:139], v[60:61], v[12:13] op_sel:[0,1,0]
	v_pk_fma_f32 v[26:27], v[140:141], v[66:67], v[26:27] op_sel_hi:[1,0,1]
	v_pk_fma_f32 v[24:25], v[138:139], v[66:67], v[24:25] op_sel_hi:[1,0,1]
	v_pk_fma_f32 v[10:11], v[140:141], v[62:63], v[10:11] op_sel_hi:[1,0,1]
	v_pk_fma_f32 v[8:9], v[138:139], v[62:63], v[8:9] op_sel_hi:[1,0,1]
	v_pk_fma_f32 v[22:23], v[140:141], v[162:163], v[22:23] op_sel_hi:[1,0,1]
	v_pk_fma_f32 v[20:21], v[138:139], v[162:163], v[20:21] op_sel_hi:[1,0,1]
	v_pk_fma_f32 v[6:7], v[140:141], v[164:165], v[6:7] op_sel_hi:[1,0,1]
	v_pk_fma_f32 v[4:5], v[138:139], v[164:165], v[4:5] op_sel_hi:[1,0,1]
	v_pk_fma_f32 v[34:35], v[144:145], v[72:73], v[34:35] op_sel_hi:[1,0,1]
	v_pk_fma_f32 v[32:33], v[142:143], v[72:73], v[32:33] op_sel_hi:[1,0,1]
	v_pk_fma_f32 v[18:19], v[144:145], v[68:69], v[18:19] op_sel_hi:[1,0,1]
	v_pk_fma_f32 v[16:17], v[142:143], v[68:69], v[16:17] op_sel_hi:[1,0,1]
	v_pk_fma_f32 v[30:31], v[144:145], v[72:73], v[30:31] op_sel:[0,1,0]
	v_pk_fma_f32 v[28:29], v[142:143], v[72:73], v[28:29] op_sel:[0,1,0]
	v_pk_fma_f32 v[14:15], v[144:145], v[68:69], v[14:15] op_sel:[0,1,0]
	v_pk_fma_f32 v[12:13], v[142:143], v[68:69], v[12:13] op_sel:[0,1,0]
	v_pk_fma_f32 v[26:27], v[144:145], v[74:75], v[26:27] op_sel_hi:[1,0,1]
	v_pk_fma_f32 v[24:25], v[142:143], v[74:75], v[24:25] op_sel_hi:[1,0,1]
	v_pk_fma_f32 v[10:11], v[144:145], v[70:71], v[10:11] op_sel_hi:[1,0,1]
	v_pk_fma_f32 v[8:9], v[142:143], v[70:71], v[8:9] op_sel_hi:[1,0,1]
	v_pk_fma_f32 v[22:23], v[144:145], v[166:167], v[22:23] op_sel_hi:[1,0,1]
	v_pk_fma_f32 v[20:21], v[142:143], v[166:167], v[20:21] op_sel_hi:[1,0,1]
	v_pk_fma_f32 v[6:7], v[144:145], v[168:169], v[6:7] op_sel_hi:[1,0,1]
	v_pk_fma_f32 v[4:5], v[142:143], v[168:169], v[4:5] op_sel_hi:[1,0,1]
	v_pk_fma_f32 v[34:35], v[148:149], v[80:81], v[34:35] op_sel_hi:[1,0,1]
	v_pk_fma_f32 v[32:33], v[146:147], v[80:81], v[32:33] op_sel_hi:[1,0,1]
	v_pk_fma_f32 v[18:19], v[148:149], v[76:77], v[18:19] op_sel_hi:[1,0,1]
	v_pk_fma_f32 v[16:17], v[146:147], v[76:77], v[16:17] op_sel_hi:[1,0,1]
	v_pk_fma_f32 v[30:31], v[148:149], v[80:81], v[30:31] op_sel:[0,1,0]
	v_pk_fma_f32 v[28:29], v[146:147], v[80:81], v[28:29] op_sel:[0,1,0]
	v_pk_fma_f32 v[14:15], v[148:149], v[76:77], v[14:15] op_sel:[0,1,0]
	v_pk_fma_f32 v[12:13], v[146:147], v[76:77], v[12:13] op_sel:[0,1,0]
	v_pk_fma_f32 v[26:27], v[148:149], v[82:83], v[26:27] op_sel_hi:[1,0,1]
	v_pk_fma_f32 v[24:25], v[146:147], v[82:83], v[24:25] op_sel_hi:[1,0,1]
	v_pk_fma_f32 v[10:11], v[148:149], v[78:79], v[10:11] op_sel_hi:[1,0,1]
	v_pk_fma_f32 v[8:9], v[146:147], v[78:79], v[8:9] op_sel_hi:[1,0,1]
	v_pk_fma_f32 v[22:23], v[148:149], v[170:171], v[22:23] op_sel_hi:[1,0,1]
	v_pk_fma_f32 v[20:21], v[146:147], v[170:171], v[20:21] op_sel_hi:[1,0,1]
	v_pk_fma_f32 v[6:7], v[148:149], v[172:173], v[6:7] op_sel_hi:[1,0,1]
	v_pk_fma_f32 v[4:5], v[146:147], v[172:173], v[4:5] op_sel_hi:[1,0,1]
	v_pk_fma_f32 v[34:35], v[152:153], v[88:89], v[34:35] op_sel_hi:[1,0,1]
	v_pk_fma_f32 v[32:33], v[150:151], v[88:89], v[32:33] op_sel_hi:[1,0,1]
	v_pk_fma_f32 v[18:19], v[152:153], v[84:85], v[18:19] op_sel_hi:[1,0,1]
	v_pk_fma_f32 v[16:17], v[150:151], v[84:85], v[16:17] op_sel_hi:[1,0,1]
	v_pk_fma_f32 v[30:31], v[152:153], v[88:89], v[30:31] op_sel:[0,1,0]
	v_pk_fma_f32 v[28:29], v[150:151], v[88:89], v[28:29] op_sel:[0,1,0]
	v_pk_fma_f32 v[14:15], v[152:153], v[84:85], v[14:15] op_sel:[0,1,0]
	v_pk_fma_f32 v[12:13], v[150:151], v[84:85], v[12:13] op_sel:[0,1,0]
	v_pk_fma_f32 v[26:27], v[152:153], v[90:91], v[26:27] op_sel_hi:[1,0,1]
	v_pk_fma_f32 v[24:25], v[150:151], v[90:91], v[24:25] op_sel_hi:[1,0,1]
	v_pk_fma_f32 v[10:11], v[152:153], v[86:87], v[10:11] op_sel_hi:[1,0,1]
	v_pk_fma_f32 v[8:9], v[150:151], v[86:87], v[8:9] op_sel_hi:[1,0,1]
	v_pk_fma_f32 v[22:23], v[152:153], v[174:175], v[22:23] op_sel_hi:[1,0,1]
	v_pk_fma_f32 v[20:21], v[150:151], v[174:175], v[20:21] op_sel_hi:[1,0,1]
	v_pk_fma_f32 v[6:7], v[152:153], v[176:177], v[6:7] op_sel_hi:[1,0,1]
	v_pk_fma_f32 v[4:5], v[150:151], v[176:177], v[4:5] op_sel_hi:[1,0,1]
	v_pk_fma_f32 v[34:35], v[42:43], v[114:115], v[34:35] op_sel_hi:[1,0,1]
	v_pk_fma_f32 v[32:33], v[40:41], v[114:115], v[32:33] op_sel_hi:[1,0,1]
	v_pk_fma_f32 v[18:19], v[42:43], v[118:119], v[18:19] op_sel_hi:[1,0,1]
	v_pk_fma_f32 v[16:17], v[40:41], v[118:119], v[16:17] op_sel_hi:[1,0,1]
	v_pk_fma_f32 v[30:31], v[42:43], v[114:115], v[30:31] op_sel:[0,1,0]
	v_pk_fma_f32 v[28:29], v[40:41], v[114:115], v[28:29] op_sel:[0,1,0]
	v_pk_fma_f32 v[14:15], v[42:43], v[118:119], v[14:15] op_sel:[0,1,0]
	v_pk_fma_f32 v[12:13], v[40:41], v[118:119], v[12:13] op_sel:[0,1,0]
	v_pk_fma_f32 v[26:27], v[42:43], v[116:117], v[26:27] op_sel_hi:[1,0,1]
	v_pk_fma_f32 v[24:25], v[40:41], v[116:117], v[24:25] op_sel_hi:[1,0,1]
	v_pk_fma_f32 v[10:11], v[42:43], v[120:121], v[10:11] op_sel_hi:[1,0,1]
	v_pk_fma_f32 v[8:9], v[40:41], v[120:121], v[8:9] op_sel_hi:[1,0,1]
	v_pk_fma_f32 v[22:23], v[42:43], v[178:179], v[22:23] op_sel_hi:[1,0,1]
	v_pk_fma_f32 v[20:21], v[40:41], v[178:179], v[20:21] op_sel_hi:[1,0,1]
	v_pk_fma_f32 v[6:7], v[42:43], v[180:181], v[6:7] op_sel_hi:[1,0,1]
	v_pk_fma_f32 v[4:5], v[40:41], v[180:181], v[4:5] op_sel_hi:[1,0,1]
	v_pk_fma_f32 v[34:35], v[38:39], v[122:123], v[34:35] op_sel_hi:[1,0,1]
	v_pk_fma_f32 v[32:33], v[36:37], v[122:123], v[32:33] op_sel_hi:[1,0,1]
	v_pk_fma_f32 v[18:19], v[38:39], v[126:127], v[18:19] op_sel_hi:[1,0,1]
	v_pk_fma_f32 v[16:17], v[36:37], v[126:127], v[16:17] op_sel_hi:[1,0,1]
	v_pk_fma_f32 v[30:31], v[38:39], v[122:123], v[30:31] op_sel:[0,1,0]
	v_pk_fma_f32 v[28:29], v[36:37], v[122:123], v[28:29] op_sel:[0,1,0]
	v_pk_fma_f32 v[14:15], v[38:39], v[126:127], v[14:15] op_sel:[0,1,0]
	v_pk_fma_f32 v[12:13], v[36:37], v[126:127], v[12:13] op_sel:[0,1,0]
	v_pk_fma_f32 v[26:27], v[38:39], v[124:125], v[26:27] op_sel_hi:[1,0,1]
	v_pk_fma_f32 v[24:25], v[36:37], v[124:125], v[24:25] op_sel_hi:[1,0,1]
	v_pk_fma_f32 v[10:11], v[38:39], v[128:129], v[10:11] op_sel_hi:[1,0,1]
	v_pk_fma_f32 v[8:9], v[36:37], v[128:129], v[8:9] op_sel_hi:[1,0,1]
	v_pk_fma_f32 v[22:23], v[38:39], v[182:183], v[22:23] op_sel_hi:[1,0,1]
	v_pk_fma_f32 v[20:21], v[36:37], v[182:183], v[20:21] op_sel_hi:[1,0,1]
	v_pk_fma_f32 v[6:7], v[38:39], v[184:185], v[6:7] op_sel_hi:[1,0,1]
	v_pk_fma_f32 v[4:5], v[36:37], v[184:185], v[4:5] op_sel_hi:[1,0,1]
	s_andn2_b64 exec, exec, s[28:29]
	s_cbranch_execnz .LBB0_942
	s_or_b64 exec, exec, s[28:29]
	s_add_i32 s10, s0, 0x200
	s_cmpk_gt_u32 s0, 0x5ff
	v_lshl_add_u64 v[96:97], v[96:97], 0, s[14:15]
	s_cbranch_scc1 .LBB0_945
	s_mov_b32 s0, s10
	s_branch .LBB0_933
